# EpiM1 (silu(g)*u -> fp8) epilogue rewritten by hand: grouped exp/rcp, packed-f32 mul/add, no pair-shuffle moves (460 vs 770 instr), on top of rotary rewrite + prologue + chain DMA reorder
# speedup vs baseline: 1.0146x; 1.0061x over previous
; DI unsigned pk4_fp8(float a, float b, float c_, float d) { int w = 0; w = __builtin_amdgcn_cvt_pk_fp8_f32(clamp8(a), clamp8(b), w, false); w = __builtin_amdgcn_cvt_pk_fp8_f32(clamp8(c_), clamp8(d), w, true); return (unsigned)w; }
; DI float sigmoid64_(float x64) { return __builtin_amdgcn_rcpf(1.0f + __builtin_amdgcn_exp2f(x64 * (-LOG2E * W8_INV))); }
;     DI void operator()(const f32x4 (&acc)[2][2][4][2], const Unit& u, int wr, int wc, int fr, int fq) const {
;         asm volatile("" : "+v"(fr), "+v"(fq));
;         const int row0 = u.pm * 256 + wr * 64 + fr, col0 = u.pn * 128 + wc * 32 + 8 * fq;
; #pragma unroll
;         for (int ai = 0; ai < 2; ++ai)
; #pragma unroll
;             for (int m2 = 0; m2 < 4; m2 += 2) { u32x2 o[2];
; #pragma unroll
;                 for (int mm = 0; mm < 2; ++mm) { const int m = m2 + mm; f32x4 v0, v1;
; #pragma unroll
;                     for (int j = 0; j < 4; ++j) { const float g0 = acc[ai][0][m][0][j], g1 = acc[ai][0][m][1][j]; v0[j] = g0 * sigmoid64_(g0) * (acc[ai][1][m][0][j] * (W8_INV * W8_INV)); v1[j] = g1 * sigmoid64_(g1) * (acc[ai][1][m][1][j] * (W8_INV * W8_INV)); }
;                     o[mm].x = pk4_fp8(v0[0], v0[1], v0[2], v0[3]); o[mm].y = pk4_fp8(v1[0], v1[1], v1[2], v1[3]); }
;                 st_pair16(hm + (size_t)(row0 + ai * 128 + m2 * 16) * 1024 + col0, 16 * 1024, o[0], o[1], fq); }
.LBB0_1367:
	s_nop 15
	s_nop 15
	s_lshl_b32 s6, s90, 8
	s_add_i32 s6, s6, s68
	v_add_u32_e32 v12, s6, v237
	s_lshl_b32 s6, s54, 7
	s_or_b32 s6, s6, s80
	v_lshl_add_u32 v14, v238, 3, s6
	v_bfe_i32 v6, v238, 0, 1
	v_and_b32_e32 v10, 0x3ff8, v6
	v_mov_b32_e32 v11, v4
	v_ashrrev_i32_e32 v15, 31, v14
	v_ashrrev_i32_e32 v13, 31, v12
	v_lshlrev_b64 v[12:13], 10, v[12:13]
	v_lshl_add_u64 v[12:13], s[46:47], 0, v[12:13]
	v_lshl_add_u64 v[12:13], v[12:13], 0, v[14:15]
	v_lshl_add_u64 v[10:11], v[12:13], 0, v[10:11]
	s_mov_b32 s6, 0x8000
	s_mov_b64 s[54:55], -1
	v_mov_b32_e32 v20, 1.0
	v_mov_b32_e32 v21, 1.0
	v_mul_f32_e32 v16, 0xbcb8aa3b, v190
	v_mul_f32_e32 v17, 0xbcb8aa3b, v191
	v_mul_f32_e32 v18, 0xbcb8aa3b, v192
	v_mul_f32_e32 v19, 0xbcb8aa3b, v193
	v_exp_f32_e32 v16, v16
	v_exp_f32_e32 v17, v17
	v_exp_f32_e32 v18, v18
	v_exp_f32_e32 v19, v19
	v_pk_add_f32 v[16:17], v[16:17], v[20:21]
	v_pk_add_f32 v[18:19], v[18:19], v[20:21]
	v_rcp_f32_e32 v16, v16
	v_rcp_f32_e32 v17, v17
	v_rcp_f32_e32 v18, v18
	v_rcp_f32_e32 v19, v19
	v_pk_mul_f32 v[194:195], v[194:195], v[206:207] op_sel:[0,1] op_sel_hi:[1,1]
	v_pk_mul_f32 v[196:197], v[196:197], v[206:207] op_sel:[0,1] op_sel_hi:[1,1]
	v_pk_mul_f32 v[190:191], v[190:191], v[16:17]
	v_pk_mul_f32 v[192:193], v[192:193], v[18:19]
	v_pk_mul_f32 v[190:191], v[190:191], v[194:195]
	v_pk_mul_f32 v[192:193], v[192:193], v[196:197]
	v_med3_f32 v190, v190, s35, v225
	v_med3_f32 v191, v191, s35, v225
	v_med3_f32 v192, v192, s35, v225
	v_med3_f32 v193, v193, s35, v225
	v_mul_f32_e32 v16, 0xbcb8aa3b, v182
	v_mul_f32_e32 v17, 0xbcb8aa3b, v183
	v_mul_f32_e32 v18, 0xbcb8aa3b, v184
	v_mul_f32_e32 v19, 0xbcb8aa3b, v185
	v_exp_f32_e32 v16, v16
	v_exp_f32_e32 v17, v17
	v_exp_f32_e32 v18, v18
	v_exp_f32_e32 v19, v19
	v_pk_add_f32 v[16:17], v[16:17], v[20:21]
	v_pk_add_f32 v[18:19], v[18:19], v[20:21]
	v_rcp_f32_e32 v16, v16
	v_rcp_f32_e32 v17, v17
	v_rcp_f32_e32 v18, v18
	v_rcp_f32_e32 v19, v19
	v_pk_mul_f32 v[186:187], v[186:187], v[206:207] op_sel:[0,1] op_sel_hi:[1,1]
	v_pk_mul_f32 v[188:189], v[188:189], v[206:207] op_sel:[0,1] op_sel_hi:[1,1]
	v_pk_mul_f32 v[182:183], v[182:183], v[16:17]
	v_pk_mul_f32 v[184:185], v[184:185], v[18:19]
	v_pk_mul_f32 v[182:183], v[182:183], v[186:187]
	v_pk_mul_f32 v[184:185], v[184:185], v[188:189]
	v_med3_f32 v182, v182, s35, v225
	v_med3_f32 v183, v183, s35, v225
	v_med3_f32 v184, v184, s35, v225
	v_med3_f32 v185, v185, s35, v225
	v_mul_f32_e32 v16, 0xbcb8aa3b, v174
	v_mul_f32_e32 v17, 0xbcb8aa3b, v175
	v_mul_f32_e32 v18, 0xbcb8aa3b, v176
	v_mul_f32_e32 v19, 0xbcb8aa3b, v177
	v_exp_f32_e32 v16, v16
	v_exp_f32_e32 v17, v17
	v_exp_f32_e32 v18, v18
	v_exp_f32_e32 v19, v19
	v_pk_add_f32 v[16:17], v[16:17], v[20:21]
	v_pk_add_f32 v[18:19], v[18:19], v[20:21]
	v_rcp_f32_e32 v16, v16
	v_rcp_f32_e32 v17, v17
	v_rcp_f32_e32 v18, v18
	v_rcp_f32_e32 v19, v19
	v_pk_mul_f32 v[178:179], v[178:179], v[206:207] op_sel:[0,1] op_sel_hi:[1,1]
	v_pk_mul_f32 v[180:181], v[180:181], v[206:207] op_sel:[0,1] op_sel_hi:[1,1]
	v_pk_mul_f32 v[174:175], v[174:175], v[16:17]
	v_pk_mul_f32 v[176:177], v[176:177], v[18:19]
	v_pk_mul_f32 v[174:175], v[174:175], v[178:179]
	v_pk_mul_f32 v[176:177], v[176:177], v[180:181]
	v_med3_f32 v174, v174, s35, v225
	v_med3_f32 v175, v175, s35, v225
	v_med3_f32 v176, v176, s35, v225
	v_med3_f32 v177, v177, s35, v225
	v_mul_f32_e32 v16, 0xbcb8aa3b, v166
	v_mul_f32_e32 v17, 0xbcb8aa3b, v167
	v_mul_f32_e32 v18, 0xbcb8aa3b, v168
	v_mul_f32_e32 v19, 0xbcb8aa3b, v169
	v_exp_f32_e32 v16, v16
	v_exp_f32_e32 v17, v17
	v_exp_f32_e32 v18, v18
	v_exp_f32_e32 v19, v19
	v_pk_add_f32 v[16:17], v[16:17], v[20:21]
	v_pk_add_f32 v[18:19], v[18:19], v[20:21]
	v_rcp_f32_e32 v16, v16
	v_rcp_f32_e32 v17, v17
	v_rcp_f32_e32 v18, v18
	v_rcp_f32_e32 v19, v19
	v_pk_mul_f32 v[170:171], v[170:171], v[206:207] op_sel:[0,1] op_sel_hi:[1,1]
	v_pk_mul_f32 v[172:173], v[172:173], v[206:207] op_sel:[0,1] op_sel_hi:[1,1]
	v_pk_mul_f32 v[166:167], v[166:167], v[16:17]
	v_pk_mul_f32 v[168:169], v[168:169], v[18:19]
	v_pk_mul_f32 v[166:167], v[166:167], v[170:171]
	v_pk_mul_f32 v[168:169], v[168:169], v[172:173]
	v_med3_f32 v166, v166, s35, v225
	v_med3_f32 v167, v167, s35, v225
	v_med3_f32 v168, v168, s35, v225
	v_med3_f32 v169, v169, s35, v225
	v_cvt_pk_fp8_f32 v190, v190, v191
	v_cvt_pk_fp8_f32 v191, v182, v183
	v_cvt_pk_fp8_f32 v190, v192, v193 op_sel:[0,0,1]
	v_cvt_pk_fp8_f32 v191, v184, v185 op_sel:[0,0,1]
	v_cvt_pk_fp8_f32 v192, v174, v175
	v_cvt_pk_fp8_f32 v193, v166, v167
	v_cvt_pk_fp8_f32 v192, v176, v177 op_sel:[0,0,1]
	v_cvt_pk_fp8_f32 v193, v168, v169 op_sel:[0,0,1]
	s_nop 1
	v_permlane16_swap_b32_e32 v190, v192
	v_permlane16_swap_b32_e32 v191, v193
	global_store_dwordx4 v[10:11], v[190:193], off
	v_mul_f32_e32 v16, 0xbcb8aa3b, v158
	v_mul_f32_e32 v17, 0xbcb8aa3b, v159
	v_mul_f32_e32 v18, 0xbcb8aa3b, v160
	v_mul_f32_e32 v19, 0xbcb8aa3b, v161
	v_exp_f32_e32 v16, v16
	v_exp_f32_e32 v17, v17
	v_exp_f32_e32 v18, v18
	v_exp_f32_e32 v19, v19
	v_pk_add_f32 v[16:17], v[16:17], v[20:21]
	v_pk_add_f32 v[18:19], v[18:19], v[20:21]
	v_rcp_f32_e32 v16, v16
	v_rcp_f32_e32 v17, v17
	v_rcp_f32_e32 v18, v18
	v_rcp_f32_e32 v19, v19
	v_pk_mul_f32 v[162:163], v[162:163], v[206:207] op_sel:[0,1] op_sel_hi:[1,1]
	v_pk_mul_f32 v[164:165], v[164:165], v[206:207] op_sel:[0,1] op_sel_hi:[1,1]
	v_pk_mul_f32 v[158:159], v[158:159], v[16:17]
	v_pk_mul_f32 v[160:161], v[160:161], v[18:19]
	v_pk_mul_f32 v[158:159], v[158:159], v[162:163]
	v_pk_mul_f32 v[160:161], v[160:161], v[164:165]
	v_med3_f32 v158, v158, s35, v225
	v_med3_f32 v159, v159, s35, v225
	v_med3_f32 v160, v160, s35, v225
	v_med3_f32 v161, v161, s35, v225
; DI unsigned pk4_fp8(float a, float b, float c_, float d) { int w = 0; w = __builtin_amdgcn_cvt_pk_fp8_f32(clamp8(a), clamp8(b), w, false); w = __builtin_amdgcn_cvt_pk_fp8_f32(clamp8(c_), clamp8(d), w, true); return (unsigned)w; }
; DI float sigmoid64_(float x64) { return __builtin_amdgcn_rcpf(1.0f + __builtin_amdgcn_exp2f(x64 * (-LOG2E * W8_INV))); }
;     DI void operator()(const f32x4 (&acc)[2][2][4][2], const Unit& u, int wr, int wc, int fr, int fq) const {
;         asm volatile("" : "+v"(fr), "+v"(fq));
;         const int row0 = u.pm * 256 + wr * 64 + fr, col0 = u.pn * 128 + wc * 32 + 8 * fq;
; #pragma unroll
;         for (int ai = 0; ai < 2; ++ai)
; #pragma unroll
;             for (int m2 = 0; m2 < 4; m2 += 2) { u32x2 o[2];
; #pragma unroll
;                 for (int mm = 0; mm < 2; ++mm) { const int m = m2 + mm; f32x4 v0, v1;
; #pragma unroll
;                     for (int j = 0; j < 4; ++j) { const float g0 = acc[ai][0][m][0][j], g1 = acc[ai][0][m][1][j]; v0[j] = g0 * sigmoid64_(g0) * (acc[ai][1][m][0][j] * (W8_INV * W8_INV)); v1[j] = g1 * sigmoid64_(g1) * (acc[ai][1][m][1][j] * (W8_INV * W8_INV)); }
;                     o[mm].x = pk4_fp8(v0[0], v0[1], v0[2], v0[3]); o[mm].y = pk4_fp8(v1[0], v1[1], v1[2], v1[3]); }
;                 st_pair16(hm + (size_t)(row0 + ai * 128 + m2 * 16) * 1024 + col0, 16 * 1024, o[0], o[1], fq); }
	v_mul_f32_e32 v16, 0xbcb8aa3b, v150
	v_mul_f32_e32 v17, 0xbcb8aa3b, v151
	v_mul_f32_e32 v18, 0xbcb8aa3b, v152
	v_mul_f32_e32 v19, 0xbcb8aa3b, v153
	v_exp_f32_e32 v16, v16
	v_exp_f32_e32 v17, v17
	v_exp_f32_e32 v18, v18
	v_exp_f32_e32 v19, v19
	v_pk_add_f32 v[16:17], v[16:17], v[20:21]
	v_pk_add_f32 v[18:19], v[18:19], v[20:21]
	v_rcp_f32_e32 v16, v16
	v_rcp_f32_e32 v17, v17
	v_rcp_f32_e32 v18, v18
	v_rcp_f32_e32 v19, v19
	v_pk_mul_f32 v[154:155], v[154:155], v[206:207] op_sel:[0,1] op_sel_hi:[1,1]
	v_pk_mul_f32 v[156:157], v[156:157], v[206:207] op_sel:[0,1] op_sel_hi:[1,1]
	v_pk_mul_f32 v[150:151], v[150:151], v[16:17]
	v_pk_mul_f32 v[152:153], v[152:153], v[18:19]
	v_pk_mul_f32 v[150:151], v[150:151], v[154:155]
	v_pk_mul_f32 v[152:153], v[152:153], v[156:157]
	v_med3_f32 v150, v150, s35, v225
	v_med3_f32 v151, v151, s35, v225
	v_med3_f32 v152, v152, s35, v225
	v_med3_f32 v153, v153, s35, v225
	v_mul_f32_e32 v16, 0xbcb8aa3b, v142
	v_mul_f32_e32 v17, 0xbcb8aa3b, v143
	v_mul_f32_e32 v18, 0xbcb8aa3b, v144
	v_mul_f32_e32 v19, 0xbcb8aa3b, v145
	v_exp_f32_e32 v16, v16
	v_exp_f32_e32 v17, v17
	v_exp_f32_e32 v18, v18
	v_exp_f32_e32 v19, v19
	v_pk_add_f32 v[16:17], v[16:17], v[20:21]
	v_pk_add_f32 v[18:19], v[18:19], v[20:21]
	v_rcp_f32_e32 v16, v16
	v_rcp_f32_e32 v17, v17
	v_rcp_f32_e32 v18, v18
	v_rcp_f32_e32 v19, v19
	v_pk_mul_f32 v[146:147], v[146:147], v[206:207] op_sel:[0,1] op_sel_hi:[1,1]
	v_pk_mul_f32 v[148:149], v[148:149], v[206:207] op_sel:[0,1] op_sel_hi:[1,1]
	v_pk_mul_f32 v[142:143], v[142:143], v[16:17]
	v_pk_mul_f32 v[144:145], v[144:145], v[18:19]
	v_pk_mul_f32 v[142:143], v[142:143], v[146:147]
	v_pk_mul_f32 v[144:145], v[144:145], v[148:149]
	v_med3_f32 v142, v142, s35, v225
	v_med3_f32 v143, v143, s35, v225
	v_med3_f32 v144, v144, s35, v225
	v_med3_f32 v145, v145, s35, v225
	v_mul_f32_e32 v16, 0xbcb8aa3b, v134
	v_mul_f32_e32 v17, 0xbcb8aa3b, v135
	v_mul_f32_e32 v18, 0xbcb8aa3b, v136
	v_mul_f32_e32 v19, 0xbcb8aa3b, v137
	v_exp_f32_e32 v16, v16
	v_exp_f32_e32 v17, v17
	v_exp_f32_e32 v18, v18
	v_exp_f32_e32 v19, v19
	v_pk_add_f32 v[16:17], v[16:17], v[20:21]
	v_pk_add_f32 v[18:19], v[18:19], v[20:21]
	v_rcp_f32_e32 v16, v16
	v_rcp_f32_e32 v17, v17
	v_rcp_f32_e32 v18, v18
	v_rcp_f32_e32 v19, v19
	v_pk_mul_f32 v[138:139], v[138:139], v[206:207] op_sel:[0,1] op_sel_hi:[1,1]
	v_pk_mul_f32 v[140:141], v[140:141], v[206:207] op_sel:[0,1] op_sel_hi:[1,1]
	v_pk_mul_f32 v[134:135], v[134:135], v[16:17]
	v_pk_mul_f32 v[136:137], v[136:137], v[18:19]
	v_pk_mul_f32 v[134:135], v[134:135], v[138:139]
	v_pk_mul_f32 v[136:137], v[136:137], v[140:141]
	v_med3_f32 v134, v134, s35, v225
	v_med3_f32 v135, v135, s35, v225
	v_med3_f32 v136, v136, s35, v225
	v_med3_f32 v137, v137, s35, v225
	v_cvt_pk_fp8_f32 v158, v158, v159
	v_cvt_pk_fp8_f32 v159, v150, v151
	v_cvt_pk_fp8_f32 v158, v160, v161 op_sel:[0,0,1]
	v_cvt_pk_fp8_f32 v159, v152, v153 op_sel:[0,0,1]
	v_cvt_pk_fp8_f32 v160, v142, v143
	v_cvt_pk_fp8_f32 v161, v134, v135
	v_cvt_pk_fp8_f32 v160, v144, v145 op_sel:[0,0,1]
	v_cvt_pk_fp8_f32 v161, v136, v137 op_sel:[0,0,1]
	v_add_co_u32_e32 v12, vcc, 0x8000, v10
	s_nop 0
	v_permlane16_swap_b32_e32 v158, v160
	v_addc_co_u32_e32 v13, vcc, 0, v11, vcc
	v_permlane16_swap_b32_e32 v159, v161
	global_store_dwordx4 v[12:13], v[158:161], off
	v_mul_f32_e32 v16, 0xbcb8aa3b, v126
	v_mul_f32_e32 v17, 0xbcb8aa3b, v127
	v_mul_f32_e32 v18, 0xbcb8aa3b, v128
	v_mul_f32_e32 v19, 0xbcb8aa3b, v129
	v_exp_f32_e32 v16, v16
	v_exp_f32_e32 v17, v17
	v_exp_f32_e32 v18, v18
	v_exp_f32_e32 v19, v19
	v_pk_add_f32 v[16:17], v[16:17], v[20:21]
	v_pk_add_f32 v[18:19], v[18:19], v[20:21]
	v_rcp_f32_e32 v16, v16
	v_rcp_f32_e32 v17, v17
	v_rcp_f32_e32 v18, v18
	v_rcp_f32_e32 v19, v19
	v_pk_mul_f32 v[130:131], v[130:131], v[206:207] op_sel:[0,1] op_sel_hi:[1,1]
	v_pk_mul_f32 v[132:133], v[132:133], v[206:207] op_sel:[0,1] op_sel_hi:[1,1]
	v_pk_mul_f32 v[126:127], v[126:127], v[16:17]
	v_pk_mul_f32 v[128:129], v[128:129], v[18:19]
	v_pk_mul_f32 v[126:127], v[126:127], v[130:131]
	v_pk_mul_f32 v[128:129], v[128:129], v[132:133]
	v_med3_f32 v126, v126, s35, v225
	v_med3_f32 v127, v127, s35, v225
	v_med3_f32 v128, v128, s35, v225
	v_med3_f32 v129, v129, s35, v225
	v_mul_f32_e32 v16, 0xbcb8aa3b, v118
	v_mul_f32_e32 v17, 0xbcb8aa3b, v119
	v_mul_f32_e32 v18, 0xbcb8aa3b, v120
	v_mul_f32_e32 v19, 0xbcb8aa3b, v121
	v_exp_f32_e32 v16, v16
	v_exp_f32_e32 v17, v17
	v_exp_f32_e32 v18, v18
	v_exp_f32_e32 v19, v19
	v_pk_add_f32 v[16:17], v[16:17], v[20:21]
	v_pk_add_f32 v[18:19], v[18:19], v[20:21]
	v_rcp_f32_e32 v16, v16
	v_rcp_f32_e32 v17, v17
	v_rcp_f32_e32 v18, v18
	v_rcp_f32_e32 v19, v19
	v_pk_mul_f32 v[122:123], v[122:123], v[206:207] op_sel:[0,1] op_sel_hi:[1,1]
	v_pk_mul_f32 v[124:125], v[124:125], v[206:207] op_sel:[0,1] op_sel_hi:[1,1]
	v_pk_mul_f32 v[118:119], v[118:119], v[16:17]
	v_pk_mul_f32 v[120:121], v[120:121], v[18:19]
	v_pk_mul_f32 v[118:119], v[118:119], v[122:123]
	v_pk_mul_f32 v[120:121], v[120:121], v[124:125]
	v_med3_f32 v118, v118, s35, v225
	v_med3_f32 v119, v119, s35, v225
	v_med3_f32 v120, v120, s35, v225
	v_med3_f32 v121, v121, s35, v225
	v_mul_f32_e32 v16, 0xbcb8aa3b, v110
	v_mul_f32_e32 v17, 0xbcb8aa3b, v111
	v_mul_f32_e32 v18, 0xbcb8aa3b, v112
	v_mul_f32_e32 v19, 0xbcb8aa3b, v113
	v_exp_f32_e32 v16, v16
	v_exp_f32_e32 v17, v17
	v_exp_f32_e32 v18, v18
	v_exp_f32_e32 v19, v19
	v_pk_add_f32 v[16:17], v[16:17], v[20:21]
	v_pk_add_f32 v[18:19], v[18:19], v[20:21]
	v_rcp_f32_e32 v16, v16
	v_rcp_f32_e32 v17, v17
	v_rcp_f32_e32 v18, v18
	v_rcp_f32_e32 v19, v19
	v_pk_mul_f32 v[114:115], v[114:115], v[206:207] op_sel:[0,1] op_sel_hi:[1,1]
; DI unsigned pk4_fp8(float a, float b, float c_, float d) { int w = 0; w = __builtin_amdgcn_cvt_pk_fp8_f32(clamp8(a), clamp8(b), w, false); w = __builtin_amdgcn_cvt_pk_fp8_f32(clamp8(c_), clamp8(d), w, true); return (unsigned)w; }
; DI float sigmoid64_(float x64) { return __builtin_amdgcn_rcpf(1.0f + __builtin_amdgcn_exp2f(x64 * (-LOG2E * W8_INV))); }
; #define PG8_BAR __builtin_amdgcn_s_barrier()
; template <class Epi, class Sched, bool F8 = false>
; DI void gemm_phase(LAS unsigned char* lds, const int K, const Sched& S, const Epi& E) {
;     ...
;         cur = nxt; cA = nA; cB = nB; ++ui;
;         if (wr == 1) PG8_BAR;
;     DI void operator()(const f32x4 (&acc)[2][2][4][2], const Unit& u, int wr, int wc, int fr, int fq) const {
;         asm volatile("" : "+v"(fr), "+v"(fq));
;         const int row0 = u.pm * 256 + wr * 64 + fr, col0 = u.pn * 128 + wc * 32 + 8 * fq;
; #pragma unroll
;         for (int ai = 0; ai < 2; ++ai)
; #pragma unroll
;             for (int m2 = 0; m2 < 4; m2 += 2) { u32x2 o[2];
; #pragma unroll
;                 for (int mm = 0; mm < 2; ++mm) { const int m = m2 + mm; f32x4 v0, v1;
; #pragma unroll
;                     for (int j = 0; j < 4; ++j) { const float g0 = acc[ai][0][m][0][j], g1 = acc[ai][0][m][1][j]; v0[j] = g0 * sigmoid64_(g0) * (acc[ai][1][m][0][j] * (W8_INV * W8_INV)); v1[j] = g1 * sigmoid64_(g1) * (acc[ai][1][m][1][j] * (W8_INV * W8_INV)); }
;                     o[mm].x = pk4_fp8(v0[0], v0[1], v0[2], v0[3]); o[mm].y = pk4_fp8(v1[0], v1[1], v1[2], v1[3]); }
;                 st_pair16(hm + (size_t)(row0 + ai * 128 + m2 * 16) * 1024 + col0, 16 * 1024, o[0], o[1], fq); }
	v_pk_mul_f32 v[116:117], v[116:117], v[206:207] op_sel:[0,1] op_sel_hi:[1,1]
	v_pk_mul_f32 v[110:111], v[110:111], v[16:17]
	v_pk_mul_f32 v[112:113], v[112:113], v[18:19]
	v_pk_mul_f32 v[110:111], v[110:111], v[114:115]
	v_pk_mul_f32 v[112:113], v[112:113], v[116:117]
	v_med3_f32 v110, v110, s35, v225
	v_med3_f32 v111, v111, s35, v225
	v_med3_f32 v112, v112, s35, v225
	v_med3_f32 v113, v113, s35, v225
	v_mul_f32_e32 v16, 0xbcb8aa3b, v102
	v_mul_f32_e32 v17, 0xbcb8aa3b, v103
	v_mul_f32_e32 v18, 0xbcb8aa3b, v104
	v_mul_f32_e32 v19, 0xbcb8aa3b, v105
	v_exp_f32_e32 v16, v16
	v_exp_f32_e32 v17, v17
	v_exp_f32_e32 v18, v18
	v_exp_f32_e32 v19, v19
	v_pk_add_f32 v[16:17], v[16:17], v[20:21]
	v_pk_add_f32 v[18:19], v[18:19], v[20:21]
	v_rcp_f32_e32 v16, v16
	v_rcp_f32_e32 v17, v17
	v_rcp_f32_e32 v18, v18
	v_rcp_f32_e32 v19, v19
	v_pk_mul_f32 v[106:107], v[106:107], v[206:207] op_sel:[0,1] op_sel_hi:[1,1]
	v_pk_mul_f32 v[108:109], v[108:109], v[206:207] op_sel:[0,1] op_sel_hi:[1,1]
	v_pk_mul_f32 v[102:103], v[102:103], v[16:17]
	v_pk_mul_f32 v[104:105], v[104:105], v[18:19]
	v_pk_mul_f32 v[102:103], v[102:103], v[106:107]
	v_pk_mul_f32 v[104:105], v[104:105], v[108:109]
	v_med3_f32 v102, v102, s35, v225
	v_med3_f32 v103, v103, s35, v225
	v_med3_f32 v104, v104, s35, v225
	v_med3_f32 v105, v105, s35, v225
	v_cvt_pk_fp8_f32 v126, v126, v127
	v_cvt_pk_fp8_f32 v127, v118, v119
	v_cvt_pk_fp8_f32 v126, v128, v129 op_sel:[0,0,1]
	v_cvt_pk_fp8_f32 v127, v120, v121 op_sel:[0,0,1]
	v_cvt_pk_fp8_f32 v128, v110, v111
	v_cvt_pk_fp8_f32 v129, v102, v103
	v_cvt_pk_fp8_f32 v128, v112, v113 op_sel:[0,0,1]
	v_cvt_pk_fp8_f32 v129, v104, v105 op_sel:[0,0,1]
	v_add_co_u32_e32 v12, vcc, 0x20000, v10
	s_nop 0
	v_permlane16_swap_b32_e32 v126, v128
	v_addc_co_u32_e32 v13, vcc, 0, v11, vcc
	v_permlane16_swap_b32_e32 v127, v129
	global_store_dwordx4 v[12:13], v[126:129], off
	v_mul_f32_e32 v16, 0xbcb8aa3b, v94
	v_mul_f32_e32 v17, 0xbcb8aa3b, v95
	v_mul_f32_e32 v18, 0xbcb8aa3b, v96
	v_mul_f32_e32 v19, 0xbcb8aa3b, v97
	v_exp_f32_e32 v16, v16
	v_exp_f32_e32 v17, v17
	v_exp_f32_e32 v18, v18
	v_exp_f32_e32 v19, v19
	v_pk_add_f32 v[16:17], v[16:17], v[20:21]
	v_pk_add_f32 v[18:19], v[18:19], v[20:21]
	v_rcp_f32_e32 v16, v16
	v_rcp_f32_e32 v17, v17
	v_rcp_f32_e32 v18, v18
	v_rcp_f32_e32 v19, v19
	v_pk_mul_f32 v[98:99], v[98:99], v[206:207] op_sel:[0,1] op_sel_hi:[1,1]
	v_pk_mul_f32 v[100:101], v[100:101], v[206:207] op_sel:[0,1] op_sel_hi:[1,1]
	v_pk_mul_f32 v[94:95], v[94:95], v[16:17]
	v_pk_mul_f32 v[96:97], v[96:97], v[18:19]
	v_pk_mul_f32 v[94:95], v[94:95], v[98:99]
	v_pk_mul_f32 v[96:97], v[96:97], v[100:101]
	v_med3_f32 v94, v94, s35, v225
	v_med3_f32 v95, v95, s35, v225
	v_med3_f32 v96, v96, s35, v225
	v_med3_f32 v97, v97, s35, v225
	v_mul_f32_e32 v16, 0xbcb8aa3b, v86
	v_mul_f32_e32 v17, 0xbcb8aa3b, v87
	v_mul_f32_e32 v18, 0xbcb8aa3b, v88
	v_mul_f32_e32 v19, 0xbcb8aa3b, v89
	v_exp_f32_e32 v16, v16
	v_exp_f32_e32 v17, v17
	v_exp_f32_e32 v18, v18
	v_exp_f32_e32 v19, v19
	v_pk_add_f32 v[16:17], v[16:17], v[20:21]
	v_pk_add_f32 v[18:19], v[18:19], v[20:21]
	v_rcp_f32_e32 v16, v16
	v_rcp_f32_e32 v17, v17
	v_rcp_f32_e32 v18, v18
	v_rcp_f32_e32 v19, v19
	v_pk_mul_f32 v[90:91], v[90:91], v[206:207] op_sel:[0,1] op_sel_hi:[1,1]
	v_pk_mul_f32 v[92:93], v[92:93], v[206:207] op_sel:[0,1] op_sel_hi:[1,1]
	v_pk_mul_f32 v[86:87], v[86:87], v[16:17]
	v_pk_mul_f32 v[88:89], v[88:89], v[18:19]
	v_pk_mul_f32 v[86:87], v[86:87], v[90:91]
	v_pk_mul_f32 v[88:89], v[88:89], v[92:93]
	v_med3_f32 v86, v86, s35, v225
	v_med3_f32 v87, v87, s35, v225
	v_med3_f32 v88, v88, s35, v225
	v_med3_f32 v89, v89, s35, v225
	v_mul_f32_e32 v16, 0xbcb8aa3b, v78
	v_mul_f32_e32 v17, 0xbcb8aa3b, v79
	v_mul_f32_e32 v18, 0xbcb8aa3b, v80
	v_mul_f32_e32 v19, 0xbcb8aa3b, v81
	v_exp_f32_e32 v16, v16
	v_exp_f32_e32 v17, v17
	v_exp_f32_e32 v18, v18
	v_exp_f32_e32 v19, v19
	v_pk_add_f32 v[16:17], v[16:17], v[20:21]
	v_pk_add_f32 v[18:19], v[18:19], v[20:21]
	v_rcp_f32_e32 v16, v16
	v_rcp_f32_e32 v17, v17
	v_rcp_f32_e32 v18, v18
	v_rcp_f32_e32 v19, v19
	v_pk_mul_f32 v[82:83], v[82:83], v[206:207] op_sel:[0,1] op_sel_hi:[1,1]
	v_pk_mul_f32 v[84:85], v[84:85], v[206:207] op_sel:[0,1] op_sel_hi:[1,1]
	v_pk_mul_f32 v[78:79], v[78:79], v[16:17]
	v_pk_mul_f32 v[80:81], v[80:81], v[18:19]
	v_pk_mul_f32 v[78:79], v[78:79], v[82:83]
	v_pk_mul_f32 v[80:81], v[80:81], v[84:85]
	v_med3_f32 v78, v78, s35, v225
	v_med3_f32 v79, v79, s35, v225
	v_med3_f32 v80, v80, s35, v225
	v_med3_f32 v81, v81, s35, v225
	v_mul_f32_e32 v16, 0xbcb8aa3b, v70
	v_mul_f32_e32 v17, 0xbcb8aa3b, v71
	v_mul_f32_e32 v18, 0xbcb8aa3b, v72
	v_mul_f32_e32 v19, 0xbcb8aa3b, v73
	v_exp_f32_e32 v16, v16
	v_exp_f32_e32 v17, v17
	v_exp_f32_e32 v18, v18
	v_exp_f32_e32 v19, v19
	v_pk_add_f32 v[16:17], v[16:17], v[20:21]
	v_pk_add_f32 v[18:19], v[18:19], v[20:21]
	v_rcp_f32_e32 v16, v16
	v_rcp_f32_e32 v17, v17
	v_rcp_f32_e32 v18, v18
	v_rcp_f32_e32 v19, v19
	v_pk_mul_f32 v[74:75], v[74:75], v[206:207] op_sel:[0,1] op_sel_hi:[1,1]
	v_pk_mul_f32 v[76:77], v[76:77], v[206:207] op_sel:[0,1] op_sel_hi:[1,1]
	v_pk_mul_f32 v[70:71], v[70:71], v[16:17]
	v_pk_mul_f32 v[72:73], v[72:73], v[18:19]
	v_pk_mul_f32 v[70:71], v[70:71], v[74:75]
	v_pk_mul_f32 v[72:73], v[72:73], v[76:77]
	v_med3_f32 v70, v70, s35, v225
	v_med3_f32 v71, v71, s35, v225
	v_med3_f32 v72, v72, s35, v225
	v_med3_f32 v73, v73, s35, v225
	v_cvt_pk_fp8_f32 v94, v94, v95
	v_cvt_pk_fp8_f32 v95, v86, v87
	v_cvt_pk_fp8_f32 v94, v96, v97 op_sel:[0,0,1]
	v_cvt_pk_fp8_f32 v95, v88, v89 op_sel:[0,0,1]
	v_cvt_pk_fp8_f32 v96, v78, v79
	v_cvt_pk_fp8_f32 v97, v70, v71
	v_cvt_pk_fp8_f32 v96, v80, v81 op_sel:[0,0,1]
	v_cvt_pk_fp8_f32 v97, v72, v73 op_sel:[0,0,1]
	v_add_co_u32_e32 v12, vcc, 0x28000, v10
	s_nop 0
	v_permlane16_swap_b32_e32 v94, v96
	v_addc_co_u32_e32 v13, vcc, 0, v11, vcc
	v_permlane16_swap_b32_e32 v95, v97
	global_store_dwordx4 v[12:13], v[94:97], off
	s_and_b64 vcc, exec, s[40:41]
	s_cbranch_vccnz .LBB0_1356
	v_readlane_b32 s6, v255, 14
	v_readlane_b32 s7, v255, 15
	s_andn2_b64 vcc, exec, s[6:7]
	s_cbranch_vccnz .LBB0_1355
	s_barrier
	s_branch .LBB0_1355
